# P0 expert-weight conversion: first load batch of an item peeled, previous item's four stores issued behind it (counted waits no longer drain the stores)
# baseline (speedup 1.0000x reference)
; #define LAS __attribute__((address_space(3)))
; __device__ __forceinline__ int opaque_tid(int wave) { int l; asm volatile("v_mbcnt_lo_u32_b32 %0, -1, 0\n\tv_mbcnt_hi_u32_b32 %0, -1, %0" : "=v"(l)); return wave * 64 + l; }
; __global__ void __launch_bounds__(NWAVES * 64, 2) fwd_kernel(Args args) {
;     extern __shared__ __attribute__((aligned(16))) unsigned char lds[];
;     Frame F;
;     F.lds = (LAS unsigned char*)lds; F.ldsg = (char*)lds;
;     F.wave0 = __builtin_amdgcn_readfirstlane((int)(threadIdx.x >> 6));
;     F.tid = opaque_tid(F.wave0); F.lane = F.tid & 63; F.wave = F.wave0;
;     F.G = gridDim.x; F.bid = blockIdx.x; F.gw = blockIdx.x * NWAVES + F.wave; F.NGW = F.G * NWAVES;
;     F.out = args.out; F.ws = args.ws; F.ctl = (gu32*)(args.ws + WS_CTL);
;     volatile LAS unsigned* MISC = (volatile LAS unsigned*)(F.lds + MISC_OFF);
;     for (int u = F.tid; u < (LDS_BYTES - MISC_OFF) / 4; u += NWAVES * 64) MISC[u] = 0u;
_Z10fwd_kernel4Args:
	s_mov_b32 s100, 0
	s_mov_b64 s[88:89], s[0:1]
	s_load_dword s90, s[0:1], 0xe8
	v_readfirstlane_b32 s0, v0
	s_lshr_b32 s53, s0, 6
	s_andn2_b32 s0, s0, 63
	v_mbcnt_lo_u32_b32 v26, -1, 0
	v_mbcnt_hi_u32_b32 v26, -1, v26
	v_writelane_b32 v232, s0, 0
	v_add_u32_e32 v0, s0, v26
	s_add_u32 s0, s88, 0xe8
	s_addc_u32 s1, s89, 0
	v_writelane_b32 v232, s0, 1
	s_mov_b32 s73, s2
	s_nop 0
	v_writelane_b32 v232, s1, 2
	s_movk_i32 s0, 0x1000
	v_cmp_gt_i32_e32 vcc, s0, v0
	s_and_saveexec_b64 s[0:1], vcc
	s_cbranch_execz .LBB0_3
	s_lshl_b32 s2, s53, 8
	s_add_i32 s2, s2, 0
	v_lshl_add_u32 v2, v26, 2, s2
	v_add_u32_e32 v1, 0xfffffe00, v0
	v_add_u32_e32 v2, 0x20000, v2
	s_mov_b64 s[2:3], 0
	v_mov_b32_e32 v3, 0
	s_movk_i32 s4, 0xdff

; #define GAS __attribute__((address_space(1)))
; #define LAS __attribute__((address_space(3)))
; #define LDS_WAIT() asm volatile("s_waitcnt lgkmcnt(0)" ::: "memory")
; __device__ __forceinline__ unsigned pk2(float lo, float hi) { return f2bf(lo) | (f2bf(hi) << 16); }
; __device__ __forceinline__ unsigned cvt_fp8x4(float a, float b, float c, float d) { int w = __builtin_amdgcn_cvt_pk_fp8_f32(a, b, 0, false); w = __builtin_amdgcn_cvt_pk_fp8_f32(c, d, w, true); return (unsigned)w; }
; template <bool FP8> __device__ __forceinline__ void p0_transpose_item(const float* W, int K, int N, bf16_t* WT, int kind, LAS float* scr, int item, int lane) {
;     ...
;     LDS_WAIT(); asm volatile("" ::: "memory");
;     const int c = lane & 7; const int d0 = drow_map(kind, n0);
; #pragma unroll
;     for (int j = 0; j < 4; ++j) { const int n = (lane >> 3) + 8 * j; const LAS float* s = scr + (8 * c) * 33 + n;
;         if (FP8) { u32x2 o; o.x = cvt_fp8x4(s[0 * 33] * W8_SCALE, s[1 * 33] * W8_SCALE, s[2 * 33] * W8_SCALE, s[3 * 33] * W8_SCALE); o.y = cvt_fp8x4(s[4 * 33] * W8_SCALE, s[5 * 33] * W8_SCALE, s[6 * 33] * W8_SCALE, s[7 * 33] * W8_SCALE);
;             *(GAS u32x2*)((unsigned char*)WT + (size_t)(d0 + n) * K + k0 + 8 * c) = o; }
;         else { u32x4 o; o.x = pk2(s[0 * 33], s[1 * 33]); o.y = pk2(s[2 * 33], s[3 * 33]); o.z = pk2(s[4 * 33], s[5 * 33]); o.w = pk2(s[6 * 33], s[7 * 33]);
;             *(GAS u32x4*)(WT + (size_t)(d0 + n) * K + k0 + 8 * c) = o; } }
.LBB0_54:
	ds_read2_b32 v[10:11], v30 offset1:8
	ds_read2_b32 v[12:13], v30 offset0:33 offset1:41
	ds_read2_b32 v[14:15], v30 offset0:66 offset1:74
	ds_read2_b32 v[18:19], v30 offset0:99 offset1:107
	ds_read2_b32 v[20:21], v30 offset0:132 offset1:140
	ds_read2_b32 v[22:23], v30 offset0:165 offset1:173
	v_mov_b32_e32 v24, 0
	s_waitcnt lgkmcnt(5)
	v_mul_f32_e32 v10, 0x42000000, v10
	s_waitcnt lgkmcnt(4)
	v_mul_f32_e32 v12, 0x42000000, v12
	ds_read2_b32 v[42:43], v30 offset0:198 offset1:206
	ds_read2_b32 v[44:45], v30 offset0:231 offset1:239
	v_cvt_pk_fp8_f32 v24, v10, v12
	s_waitcnt lgkmcnt(3)
	v_mul_f32_e32 v10, 0x42000000, v20
	s_waitcnt lgkmcnt(2)
	v_mul_f32_e32 v12, 0x42000000, v22
	v_mov_b32_e32 v25, 0
	v_cvt_pk_fp8_f32 v25, v10, v12
	s_waitcnt lgkmcnt(1)
	v_mul_f32_e32 v10, 0x42000000, v42
	s_waitcnt lgkmcnt(0)
	v_mul_f32_e32 v12, 0x42000000, v44
	v_mul_f32_e32 v11, 0x42000000, v11
	v_cvt_pk_fp8_f32 v25, v10, v12 op_sel:[0,0,1]
	v_mul_f32_e32 v12, 0x42000000, v13
	v_mov_b32_e32 v10, 0
	v_mul_f32_e32 v13, 0x42000000, v15
	v_cvt_pk_fp8_f32 v10, v11, v12
	v_mul_f32_e32 v12, 0x42000000, v21
	v_mul_f32_e32 v15, 0x42000000, v23
	v_mov_b32_e32 v11, 0
	s_ashr_i64 s[8:9], s[4:5], 11
	v_cvt_pk_fp8_f32 v11, v12, v15
	s_add_u32 s0, s10, s8
	v_mul_f32_e32 v14, 0x42000000, v14
	v_mul_f32_e32 v18, 0x42000000, v18
	s_addc_u32 s5, s11, s9
	v_cvt_pk_fp8_f32 v24, v14, v18 op_sel:[0,0,1]
	v_mul_f32_e32 v14, 0x42000000, v19
	s_add_u32 s8, s0, s22
	v_add_u32_e32 v46, s1, v1
	v_cvt_pk_fp8_f32 v10, v13, v14 op_sel:[0,0,1]
	v_mul_f32_e32 v12, 0x42000000, v43
	v_mul_f32_e32 v13, 0x42000000, v45
	s_addc_u32 s9, s5, s24
	v_ashrrev_i32_e32 v47, 31, v46
	v_cvt_pk_fp8_f32 v11, v12, v13 op_sel:[0,0,1]
	v_add_u32_e32 v12, s1, v31
	v_lshl_add_u64 v[16:17], s[8:9], 0, v[4:5]
	v_lshlrev_b64 v[46:47], 10, v[46:47]
	v_ashrrev_i32_e32 v13, 31, v12
	v_lshl_add_u64 v[46:47], v[16:17], 0, v[46:47]
	v_lshlrev_b64 v[12:13], 10, v[12:13]
	v_mov_b64_e32 v[200:201], v[46:47]
	v_mov_b64_e32 v[202:203], v[24:25]
	v_lshl_add_u64 v[12:13], v[16:17], 0, v[12:13]
	ds_read2_b32 v[14:15], v30 offset0:16 offset1:24
	ds_read2_b32 v[18:19], v30 offset0:49 offset1:57
	ds_read2_b32 v[20:21], v30 offset0:82 offset1:90
	v_mov_b64_e32 v[204:205], v[12:13]
	v_mov_b64_e32 v[206:207], v[10:11]
	ds_read2_b32 v[10:11], v30 offset0:115 offset1:123
	ds_read2_b32 v[12:13], v30 offset0:148 offset1:156
	ds_read2_b32 v[22:23], v30 offset0:181 offset1:189
	s_waitcnt lgkmcnt(5)
	v_mul_f32_e32 v14, 0x42000000, v14
	s_waitcnt lgkmcnt(4)
	v_mul_f32_e32 v18, 0x42000000, v18
	v_mov_b32_e32 v24, 0
	ds_read2_b32 v[42:43], v30 offset0:214 offset1:222
	ds_read2_b32 v[44:45], v30 offset0:247 offset1:255
	v_cvt_pk_fp8_f32 v24, v14, v18
	s_waitcnt lgkmcnt(3)
	v_mul_f32_e32 v12, 0x42000000, v12
	s_waitcnt lgkmcnt(2)
	v_mul_f32_e32 v14, 0x42000000, v22
	v_mov_b32_e32 v25, 0
	v_cvt_pk_fp8_f32 v25, v12, v14
	v_mul_f32_e32 v20, 0x42000000, v20
	v_mul_f32_e32 v10, 0x42000000, v10
	v_cvt_pk_fp8_f32 v24, v20, v10 op_sel:[0,0,1]
	s_waitcnt lgkmcnt(1)
	v_mul_f32_e32 v10, 0x42000000, v42
	s_waitcnt lgkmcnt(0)
	v_mul_f32_e32 v12, 0x42000000, v44
	v_cvt_pk_fp8_f32 v25, v10, v12 op_sel:[0,0,1]
	v_mul_f32_e32 v12, 0x42000000, v15
	v_mul_f32_e32 v14, 0x42000000, v19
	v_mov_b32_e32 v10, 0
	v_mul_f32_e32 v18, 0x42000000, v11
	v_cvt_pk_fp8_f32 v10, v12, v14
	v_mul_f32_e32 v12, 0x42000000, v13
	v_mul_f32_e32 v13, 0x42000000, v23
	v_mov_b32_e32 v11, 0
	v_cvt_pk_fp8_f32 v11, v12, v13
	v_mul_f32_e32 v15, 0x42000000, v21
	v_mul_f32_e32 v12, 0x42000000, v43
	v_mul_f32_e32 v13, 0x42000000, v45
	v_add_u32_e32 v46, s1, v32
	v_cvt_pk_fp8_f32 v10, v15, v18 op_sel:[0,0,1]
	v_cvt_pk_fp8_f32 v11, v12, v13 op_sel:[0,0,1]
	v_add_u32_e32 v12, s1, v33
	v_ashrrev_i32_e32 v47, 31, v46
	v_ashrrev_i32_e32 v13, 31, v12
	v_lshlrev_b64 v[46:47], 10, v[46:47]
	v_lshlrev_b64 v[12:13], 10, v[12:13]
	v_lshl_add_u64 v[46:47], v[16:17], 0, v[46:47]
	v_lshl_add_u64 v[12:13], v[16:17], 0, v[12:13]
	v_mov_b64_e32 v[208:209], v[46:47]
	v_mov_b64_e32 v[210:211], v[24:25]
	v_mov_b64_e32 v[212:213], v[12:13]
	v_mov_b64_e32 v[214:215], v[10:11]
	s_mov_b32 s100, 1
	s_waitcnt lgkmcnt(0)
	s_add_u32 s6, s6, s2
	s_addc_u32 s7, s7, s3
	v_cmp_lt_i64_e32 vcc, s[6:7], v[8:9]
	s_cbranch_vccz .LBB0_61
; #define LDS_WAIT() asm volatile("s_waitcnt lgkmcnt(0)" ::: "memory")
; template <bool FP8> __device__ __forceinline__ void p0_transpose_item(const float* W, int K, int N, bf16_t* WT, int kind, LAS float* scr, int item, int lane) {
;     const int nblk = N / 32, kb = item / nblk, nb = item % nblk, k0 = 64 * kb, n0 = 32 * nb;
; #pragma unroll 8
;     for (int i = 0; i < 32; ++i) { const int kk = 2 * i + (lane >> 5); scr[kk * 33 + (lane & 31)] = __builtin_nontemporal_load(&W[(size_t)(k0 + kk) * N + n0 + (lane & 31)]); }
;     LDS_WAIT(); asm volatile("" ::: "memory");
; template <bool FP8> __device__ __forceinline__ void p0_job(Frame& F, LAS float* scr, long& base, const float* src, int K, int N, int M, bf16_t* dst, int ND, int kind) {
;     ...
;     for (long it = first; it < tot; it += F.NGW) { const int mtx = (int)(it / per), loc = (int)(it % per);
;         p0_transpose_item<FP8>(src + (size_t)mtx * K * N, K, N, (bf16_t*)((unsigned char*)dst + (size_t)mtx * ND * K * (FP8 ? 1 : 2)), kind, scr, loc, F.lane); }
.LBB0_55:
	s_ashr_i32 s0, s7, 31
	s_lshr_b32 s0, s0, 22
	s_add_u32 s0, s6, s0
	s_addc_u32 s1, s7, 0
	s_ashr_i64 s[0:1], s[0:1], 10
	s_lshl_b32 s1, s0, 10
	s_sub_i32 s1, s6, s1
	s_mov_b32 s5, s0
	s_sext_i32_i16 s0, s1
	s_bfe_u32 s0, s0, 0x60019
	s_add_i32 s0, s1, s0
	s_sext_i32_i16 s12, s0
	s_and_b32 s0, s0, 0xffc0
	s_sub_i32 s0, s1, s0
	s_sext_i32_i16 s23, s0
	s_lshl_b32 s0, s23, 5
	s_ashr_i32 s1, s0, 31
	s_ashr_i64 s[8:9], s[4:5], 9
	s_and_b32 s22, s12, 0xffffffc0
	s_lshl_b64 s[24:25], s[0:1], 2
	s_add_u32 s8, s8, s24
	v_or_b32_e32 v10, s22, v35
	s_addc_u32 s9, s9, s25
	v_or_b32_e32 v12, s22, v36
	v_or_b32_e32 v14, s22, v37
	v_or_b32_e32 v16, s22, v38
	v_or_b32_e32 v18, s22, v39
	v_or_b32_e32 v20, s22, v40
	v_or_b32_e32 v22, s22, v41
	s_ashr_i32 s24, s22, 31
	v_ashrrev_i32_e32 v11, 31, v10
	v_ashrrev_i32_e32 v13, 31, v12
	v_ashrrev_i32_e32 v15, 31, v14
	v_ashrrev_i32_e32 v17, 31, v16
	v_ashrrev_i32_e32 v19, 31, v18
	v_ashrrev_i32_e32 v21, 31, v20
	v_ashrrev_i32_e32 v23, 31, v22
	v_mov_b32_e32 v25, s24
	v_or_b32_e32 v24, s22, v2
	v_lshlrev_b64 v[10:11], 13, v[10:11]
	v_lshlrev_b64 v[12:13], 13, v[12:13]
	v_lshlrev_b64 v[14:15], 13, v[14:15]
	v_lshlrev_b64 v[16:17], 13, v[16:17]
	v_lshlrev_b64 v[18:19], 13, v[18:19]
	v_lshlrev_b64 v[20:21], 13, v[20:21]
	v_lshlrev_b64 v[22:23], 13, v[22:23]
	v_lshlrev_b64 v[24:25], 13, v[24:25]
	v_lshl_add_u64 v[10:11], s[8:9], 0, v[10:11]
	v_lshl_add_u64 v[12:13], s[8:9], 0, v[12:13]
	v_lshl_add_u64 v[14:15], s[8:9], 0, v[14:15]
	v_lshl_add_u64 v[16:17], s[8:9], 0, v[16:17]
	v_lshl_add_u64 v[18:19], s[8:9], 0, v[18:19]
	v_lshl_add_u64 v[20:21], s[8:9], 0, v[20:21]
	v_lshl_add_u64 v[22:23], s[8:9], 0, v[22:23]
	v_lshl_add_u64 v[24:25], s[8:9], 0, v[24:25]
	v_lshl_add_u64 v[10:11], v[6:7], 0, v[10:11]
	v_lshl_add_u64 v[12:13], v[6:7], 0, v[12:13]
	v_lshl_add_u64 v[14:15], v[6:7], 0, v[14:15]
	v_lshl_add_u64 v[16:17], v[6:7], 0, v[16:17]
	v_lshl_add_u64 v[18:19], v[6:7], 0, v[18:19]
	v_lshl_add_u64 v[20:21], v[6:7], 0, v[20:21]
	v_lshl_add_u64 v[22:23], v[6:7], 0, v[22:23]
	v_lshl_add_u64 v[24:25], v[6:7], 0, v[24:25]
	s_mov_b64 s[8:9], 0
	v_mov_b32_e32 v42, v34
	v_lshl_add_u64 v[44:45], v[24:25], 0, s[8:9]
	v_lshl_add_u64 v[46:47], v[22:23], 0, s[8:9]
	v_lshl_add_u64 v[48:49], v[20:21], 0, s[8:9]
	v_lshl_add_u64 v[50:51], v[18:19], 0, s[8:9]
	v_lshl_add_u64 v[52:53], v[16:17], 0, s[8:9]
	v_lshl_add_u64 v[54:55], v[14:15], 0, s[8:9]
	v_lshl_add_u64 v[56:57], v[12:13], 0, s[8:9]
	v_lshl_add_u64 v[58:59], v[10:11], 0, s[8:9]
	global_load_dword v43, v[44:45], off nt
	global_load_dword v60, v[46:47], off nt
	global_load_dword v61, v[48:49], off nt
	global_load_dword v62, v[50:51], off nt
	global_load_dword v63, v[52:53], off nt
	global_load_dword v64, v[54:55], off nt
	global_load_dword v65, v[56:57], off nt
	global_load_dword v66, v[58:59], off nt
	s_cmp_eq_u32 s100, 0
	s_cbranch_scc1 .Lp0d_j56_nost
	global_store_dwordx2 v[200:201], v[202:203], off
	global_store_dwordx2 v[204:205], v[206:207], off
	global_store_dwordx2 v[208:209], v[210:211], off
	global_store_dwordx2 v[212:213], v[214:215], off
	s_branch .Lp0d_j56_go
.Lp0d_j56_nost:
	global_load_dword v251, v[44:45], off
	global_load_dword v251, v[44:45], off
	global_load_dword v251, v[44:45], off
	global_load_dword v251, v[44:45], off
.Lp0d_j56_go:
	s_add_u32 s8, s8, 0x20000
	s_addc_u32 s9, s9, 0
	v_add_u32_e32 v44, 0x400, v42
	s_cmp_eq_u32 s8, 0x80000
	s_waitcnt vmcnt(10)
	ds_write2_b32 v42, v43, v60 offset1:66
	s_waitcnt vmcnt(8)
	ds_write2_b32 v42, v61, v62 offset0:132 offset1:198
	s_waitcnt vmcnt(6)
	ds_write2_b32 v44, v63, v64 offset0:8 offset1:74
	s_waitcnt vmcnt(4)
	ds_write2_b32 v44, v65, v66 offset0:140 offset1:206
	v_add_u32_e32 v42, 0x840, v42

; #define LAS __attribute__((address_space(3)))
; template <bool FP8> __device__ __forceinline__ void p0_job(Frame& F, LAS float* scr, long& base, const float* src, int K, int N, int M, bf16_t* dst, int ND, int kind) {
;     const int per = (K / 64) * (N / 32); const long tot = (long)per * M;
;     long first = (long)F.gw - (base % F.NGW); if (first < 0) first += F.NGW;
;     for (long it = first; it < tot; it += F.NGW) { const int mtx = (int)(it / per), loc = (int)(it % per);
;         p0_transpose_item<FP8>(src + (size_t)mtx * K * N, K, N, (bf16_t*)((unsigned char*)dst + (size_t)mtx * ND * K * (FP8 ? 1 : 2)), kind, scr, loc, F.lane); }
;     base += tot;
.LBB0_61:
	s_cmp_eq_u32 s100, 0
	s_cbranch_scc1 .Lp0d_j56_done
	global_store_dwordx2 v[200:201], v[202:203], off
	global_store_dwordx2 v[204:205], v[206:207], off
	global_store_dwordx2 v[208:209], v[210:211], off
	global_store_dwordx2 v[212:213], v[214:215], off
	s_mov_b32 s100, 0

; #define LDS_WAIT() asm volatile("s_waitcnt lgkmcnt(0)" ::: "memory")
; template <bool FP8> __device__ __forceinline__ void p0_transpose_item(const float* W, int K, int N, bf16_t* WT, int kind, LAS float* scr, int item, int lane) {
;     const int nblk = N / 32, kb = item / nblk, nb = item % nblk, k0 = 64 * kb, n0 = 32 * nb;
; #pragma unroll 8
;     for (int i = 0; i < 32; ++i) { const int kk = 2 * i + (lane >> 5); scr[kk * 33 + (lane & 31)] = __builtin_nontemporal_load(&W[(size_t)(k0 + kk) * N + n0 + (lane & 31)]); }
;     LDS_WAIT(); asm volatile("" ::: "memory");
; template <bool FP8> __device__ __forceinline__ void p0_job(Frame& F, LAS float* scr, long& base, const float* src, int K, int N, int M, bf16_t* dst, int ND, int kind) {
;     ...
;     for (long it = first; it < tot; it += F.NGW) { const int mtx = (int)(it / per), loc = (int)(it % per);
;         p0_transpose_item<FP8>(src + (size_t)mtx * K * N, K, N, (bf16_t*)((unsigned char*)dst + (size_t)mtx * ND * K * (FP8 ? 1 : 2)), kind, scr, loc, F.lane); }
.LBB0_63:
	s_ashr_i32 s0, s5, 31
	s_lshr_b32 s0, s0, 23
	s_add_u32 s0, s4, s0
	s_addc_u32 s1, s5, 0
	s_ashr_i64 s[0:1], s[0:1], 9
	s_lshl_b32 s1, s0, 9
	s_sub_i32 s10, s4, s1
	s_sext_i32_i16 s11, s10
	s_bfe_u32 s11, s11, 0x5001a
	s_add_i32 s11, s10, s11
	s_sext_i32_i16 s12, s11
	s_and_b32 s11, s11, 0xffe0
	s_sub_i32 s10, s10, s11
	s_sext_i32_i16 s10, s10
	s_lshl_b32 s11, s12, 1
	s_lshl_b32 s10, s10, 5
	s_mov_b32 s7, s0
	s_and_b32 s17, s11, 0xffffffc0
	s_ashr_i32 s11, s10, 31
	s_ashr_i64 s[0:1], s[6:7], 10
	s_lshl_b64 s[18:19], s[10:11], 2
	s_add_u32 s0, s0, s18
	v_or_b32_e32 v10, s17, v33
	s_addc_u32 s1, s1, s19
	v_or_b32_e32 v12, s17, v34
	v_or_b32_e32 v14, s17, v35
	v_or_b32_e32 v16, s17, v36
	v_or_b32_e32 v18, s17, v37
	v_or_b32_e32 v20, s17, v38
	v_or_b32_e32 v22, s17, v3
	s_ashr_i32 s11, s17, 31
	v_ashrrev_i32_e32 v11, 31, v10
	v_ashrrev_i32_e32 v13, 31, v12
	v_ashrrev_i32_e32 v15, 31, v14
	v_ashrrev_i32_e32 v17, 31, v16
	v_ashrrev_i32_e32 v19, 31, v18
	v_ashrrev_i32_e32 v21, 31, v20
	v_ashrrev_i32_e32 v23, 31, v22
	v_mov_b32_e32 v25, s11
	v_or_b32_e32 v24, s17, v2
	v_lshlrev_b64 v[10:11], 12, v[10:11]
	v_lshlrev_b64 v[12:13], 12, v[12:13]
	v_lshlrev_b64 v[14:15], 12, v[14:15]
	v_lshlrev_b64 v[16:17], 12, v[16:17]
	v_lshlrev_b64 v[18:19], 12, v[18:19]
	v_lshlrev_b64 v[20:21], 12, v[20:21]
	v_lshlrev_b64 v[22:23], 12, v[22:23]
	v_lshlrev_b64 v[24:25], 12, v[24:25]
	v_lshl_add_u64 v[10:11], s[0:1], 0, v[10:11]
	v_lshl_add_u64 v[12:13], s[0:1], 0, v[12:13]
	v_lshl_add_u64 v[14:15], s[0:1], 0, v[14:15]
	v_lshl_add_u64 v[16:17], s[0:1], 0, v[16:17]
	v_lshl_add_u64 v[18:19], s[0:1], 0, v[18:19]
	v_lshl_add_u64 v[20:21], s[0:1], 0, v[20:21]
	v_lshl_add_u64 v[22:23], s[0:1], 0, v[22:23]
	v_lshl_add_u64 v[24:25], s[0:1], 0, v[24:25]
	v_lshl_add_u64 v[10:11], v[8:9], 0, v[10:11]
	v_lshl_add_u64 v[12:13], v[8:9], 0, v[12:13]
	v_lshl_add_u64 v[14:15], v[8:9], 0, v[14:15]
	v_lshl_add_u64 v[16:17], v[8:9], 0, v[16:17]
	v_lshl_add_u64 v[18:19], v[8:9], 0, v[18:19]
	v_lshl_add_u64 v[20:21], v[8:9], 0, v[20:21]
	v_lshl_add_u64 v[22:23], v[8:9], 0, v[22:23]
	v_lshl_add_u64 v[24:25], v[8:9], 0, v[24:25]
	s_mov_b64 s[0:1], 0
	v_mov_b32_e32 v39, v28
	v_lshl_add_u64 v[40:41], v[24:25], 0, s[0:1]
	v_lshl_add_u64 v[42:43], v[22:23], 0, s[0:1]
	v_lshl_add_u64 v[44:45], v[20:21], 0, s[0:1]
	v_lshl_add_u64 v[46:47], v[18:19], 0, s[0:1]
	v_lshl_add_u64 v[48:49], v[16:17], 0, s[0:1]
	v_lshl_add_u64 v[50:51], v[14:15], 0, s[0:1]
	v_lshl_add_u64 v[52:53], v[12:13], 0, s[0:1]
	v_lshl_add_u64 v[54:55], v[10:11], 0, s[0:1]
	global_load_dword v56, v[40:41], off nt
	global_load_dword v57, v[42:43], off nt
	global_load_dword v58, v[44:45], off nt
	global_load_dword v59, v[46:47], off nt
	global_load_dword v60, v[48:49], off nt
	global_load_dword v61, v[50:51], off nt
	global_load_dword v62, v[52:53], off nt
	global_load_dword v63, v[54:55], off nt
	s_cmp_eq_u32 s100, 0
	s_cbranch_scc1 .Lp0d_j64_nost
	global_store_dwordx2 v[216:217], v[218:219], off
	global_store_dwordx2 v[220:221], v[222:223], off
	global_store_dwordx2 v[224:225], v[226:227], off
	global_store_dwordx2 v[228:229], v[230:231], off
	s_branch .Lp0d_j64_go
.Lp0d_j64_nost:
	global_load_dword v251, v[40:41], off
	global_load_dword v251, v[40:41], off
	global_load_dword v251, v[40:41], off
	global_load_dword v251, v[40:41], off
.Lp0d_j64_go:
	s_add_u32 s0, s0, 0x10000
	s_addc_u32 s1, s1, 0
	v_add_u32_e32 v40, 0x400, v39
	s_cmp_eq_u32 s0, 0x40000
	s_waitcnt vmcnt(10)
	ds_write2_b32 v39, v56, v57 offset1:66
	s_waitcnt vmcnt(8)
	ds_write2_b32 v39, v58, v59 offset0:132 offset1:198
	s_waitcnt vmcnt(6)
	ds_write2_b32 v40, v60, v61 offset0:8 offset1:74
	s_waitcnt vmcnt(4)
	ds_write2_b32 v40, v62, v63 offset0:140 offset1:206
	v_add_u32_e32 v39, 0x840, v39
; #define GAS __attribute__((address_space(1)))
; #define LAS __attribute__((address_space(3)))
; #define LDS_WAIT() asm volatile("s_waitcnt lgkmcnt(0)" ::: "memory")
; __device__ __forceinline__ unsigned pk2(float lo, float hi) { return f2bf(lo) | (f2bf(hi) << 16); }
; __device__ __forceinline__ unsigned cvt_fp8x4(float a, float b, float c, float d) { int w = __builtin_amdgcn_cvt_pk_fp8_f32(a, b, 0, false); w = __builtin_amdgcn_cvt_pk_fp8_f32(c, d, w, true); return (unsigned)w; }
; template <bool FP8> __device__ __forceinline__ void p0_transpose_item(const float* W, int K, int N, bf16_t* WT, int kind, LAS float* scr, int item, int lane) {
;     ...
;     for (int i = 0; i < 32; ++i) { const int kk = 2 * i + (lane >> 5); scr[kk * 33 + (lane & 31)] = __builtin_nontemporal_load(&W[(size_t)(k0 + kk) * N + n0 + (lane & 31)]); }
;     LDS_WAIT(); asm volatile("" ::: "memory");
;     const int c = lane & 7; const int d0 = drow_map(kind, n0);
; #pragma unroll
;     for (int j = 0; j < 4; ++j) { const int n = (lane >> 3) + 8 * j; const LAS float* s = scr + (8 * c) * 33 + n;
;         if (FP8) { u32x2 o; o.x = cvt_fp8x4(s[0 * 33] * W8_SCALE, s[1 * 33] * W8_SCALE, s[2 * 33] * W8_SCALE, s[3 * 33] * W8_SCALE); o.y = cvt_fp8x4(s[4 * 33] * W8_SCALE, s[5 * 33] * W8_SCALE, s[6 * 33] * W8_SCALE, s[7 * 33] * W8_SCALE);
;             *(GAS u32x2*)((unsigned char*)WT + (size_t)(d0 + n) * K + k0 + 8 * c) = o; }
;         else { u32x4 o; o.x = pk2(s[0 * 33], s[1 * 33]); o.y = pk2(s[2 * 33], s[3 * 33]); o.z = pk2(s[4 * 33], s[5 * 33]); o.w = pk2(s[6 * 33], s[7 * 33]);
;             *(GAS u32x4*)(WT + (size_t)(d0 + n) * K + k0 + 8 * c) = o; } }
.LBB0_64:
	v_lshl_add_u64 v[40:41], v[24:25], 0, s[0:1]
	v_lshl_add_u64 v[42:43], v[22:23], 0, s[0:1]
	v_lshl_add_u64 v[44:45], v[20:21], 0, s[0:1]
	v_lshl_add_u64 v[46:47], v[18:19], 0, s[0:1]
	v_lshl_add_u64 v[48:49], v[16:17], 0, s[0:1]
	v_lshl_add_u64 v[50:51], v[14:15], 0, s[0:1]
	v_lshl_add_u64 v[52:53], v[12:13], 0, s[0:1]
	v_lshl_add_u64 v[54:55], v[10:11], 0, s[0:1]
	global_load_dword v56, v[40:41], off nt
	global_load_dword v57, v[42:43], off nt
	global_load_dword v58, v[44:45], off nt
	global_load_dword v59, v[46:47], off nt
	global_load_dword v60, v[48:49], off nt
	global_load_dword v61, v[50:51], off nt
	global_load_dword v62, v[52:53], off nt
	global_load_dword v63, v[54:55], off nt
	s_add_u32 s0, s0, 0x10000
	s_addc_u32 s1, s1, 0
	v_add_u32_e32 v40, 0x400, v39
	s_cmp_eq_u32 s0, 0x40000
	s_waitcnt vmcnt(6)
	ds_write2_b32 v39, v56, v57 offset1:66
	s_waitcnt vmcnt(4)
	ds_write2_b32 v39, v58, v59 offset0:132 offset1:198
	s_waitcnt vmcnt(2)
	ds_write2_b32 v40, v60, v61 offset0:8 offset1:74
	s_waitcnt vmcnt(0)
	ds_write2_b32 v40, v62, v63 offset0:140 offset1:206
	v_add_u32_e32 v39, 0x840, v39
	s_cbranch_scc0 .LBB0_64
	s_waitcnt lgkmcnt(0)
	ds_read2_b32 v[10:11], v29 offset1:8
	ds_read2_b32 v[12:13], v29 offset0:33 offset1:41
	ds_read2_b32 v[14:15], v29 offset0:66 offset1:74
	ds_read2_b32 v[18:19], v29 offset0:99 offset1:107
	ds_read2_b32 v[20:21], v29 offset0:132 offset1:140
	ds_read2_b32 v[22:23], v29 offset0:165 offset1:173
	v_mov_b32_e32 v24, 0
	s_waitcnt lgkmcnt(5)
	v_mul_f32_e32 v10, 0x42000000, v10
	s_waitcnt lgkmcnt(4)
	v_mul_f32_e32 v12, 0x42000000, v12
	ds_read2_b32 v[40:41], v29 offset0:198 offset1:206
	ds_read2_b32 v[42:43], v29 offset0:231 offset1:239
	v_cvt_pk_fp8_f32 v24, v10, v12
	s_waitcnt lgkmcnt(3)
	v_mul_f32_e32 v10, 0x42000000, v20
	s_waitcnt lgkmcnt(2)
	v_mul_f32_e32 v12, 0x42000000, v22
	v_mov_b32_e32 v25, 0
	v_cvt_pk_fp8_f32 v25, v10, v12
	s_waitcnt lgkmcnt(1)
	v_mul_f32_e32 v10, 0x42000000, v40
	s_waitcnt lgkmcnt(0)
	v_mul_f32_e32 v12, 0x42000000, v42
	v_mul_f32_e32 v11, 0x42000000, v11
	v_cvt_pk_fp8_f32 v25, v10, v12 op_sel:[0,0,1]
	v_mul_f32_e32 v12, 0x42000000, v13
	v_mov_b32_e32 v10, 0
	v_mul_f32_e32 v13, 0x42000000, v15
	v_cvt_pk_fp8_f32 v10, v11, v12
	v_mul_f32_e32 v12, 0x42000000, v21
	v_mul_f32_e32 v15, 0x42000000, v23
	v_mov_b32_e32 v11, 0
	s_ashr_i64 s[0:1], s[6:7], 12
	v_cvt_pk_fp8_f32 v11, v12, v15
	s_add_u32 s0, s8, s0
	v_mul_f32_e32 v14, 0x42000000, v14
	v_mul_f32_e32 v18, 0x42000000, v18
	s_addc_u32 s1, s9, s1
	v_cvt_pk_fp8_f32 v24, v14, v18 op_sel:[0,0,1]
	v_mul_f32_e32 v14, 0x42000000, v19
	s_add_u32 s0, s0, s17
	v_or_b32_e32 v44, s10, v1
	v_cvt_pk_fp8_f32 v10, v13, v14 op_sel:[0,0,1]
	v_mul_f32_e32 v12, 0x42000000, v41
	v_mul_f32_e32 v13, 0x42000000, v43
	s_addc_u32 s1, s1, s11
	v_ashrrev_i32_e32 v45, 31, v44
	v_cvt_pk_fp8_f32 v11, v12, v13 op_sel:[0,0,1]
	v_or_b32_e32 v12, s10, v30
	v_lshl_add_u64 v[16:17], s[0:1], 0, v[6:7]
	v_lshlrev_b64 v[44:45], 10, v[44:45]
	v_ashrrev_i32_e32 v13, 31, v12
	v_lshl_add_u64 v[44:45], v[16:17], 0, v[44:45]
	v_lshlrev_b64 v[12:13], 10, v[12:13]
	v_mov_b64_e32 v[216:217], v[44:45]
	v_mov_b64_e32 v[218:219], v[24:25]
	v_lshl_add_u64 v[12:13], v[16:17], 0, v[12:13]
	ds_read2_b32 v[14:15], v29 offset0:16 offset1:24
	ds_read2_b32 v[18:19], v29 offset0:49 offset1:57
	ds_read2_b32 v[20:21], v29 offset0:82 offset1:90
	v_mov_b64_e32 v[220:221], v[12:13]
	v_mov_b64_e32 v[222:223], v[10:11]
	ds_read2_b32 v[10:11], v29 offset0:115 offset1:123
	ds_read2_b32 v[12:13], v29 offset0:148 offset1:156
	ds_read2_b32 v[22:23], v29 offset0:181 offset1:189
	s_waitcnt lgkmcnt(5)
	v_mul_f32_e32 v14, 0x42000000, v14
	s_waitcnt lgkmcnt(4)
	v_mul_f32_e32 v18, 0x42000000, v18
	v_mov_b32_e32 v24, 0
	ds_read2_b32 v[40:41], v29 offset0:214 offset1:222
	ds_read2_b32 v[42:43], v29 offset0:247 offset1:255
	v_cvt_pk_fp8_f32 v24, v14, v18
	s_waitcnt lgkmcnt(3)
	v_mul_f32_e32 v12, 0x42000000, v12
	s_waitcnt lgkmcnt(2)
	v_mul_f32_e32 v14, 0x42000000, v22
	v_mov_b32_e32 v25, 0
	v_cvt_pk_fp8_f32 v25, v12, v14
	v_mul_f32_e32 v20, 0x42000000, v20
	v_mul_f32_e32 v10, 0x42000000, v10
	v_cvt_pk_fp8_f32 v24, v20, v10 op_sel:[0,0,1]
	s_waitcnt lgkmcnt(1)
	v_mul_f32_e32 v10, 0x42000000, v40
	s_waitcnt lgkmcnt(0)
	v_mul_f32_e32 v12, 0x42000000, v42
	v_cvt_pk_fp8_f32 v25, v10, v12 op_sel:[0,0,1]
	v_mul_f32_e32 v12, 0x42000000, v15
	v_mul_f32_e32 v14, 0x42000000, v19
	v_mov_b32_e32 v10, 0
	v_mul_f32_e32 v18, 0x42000000, v11
	v_cvt_pk_fp8_f32 v10, v12, v14
	v_mul_f32_e32 v12, 0x42000000, v13
	v_mul_f32_e32 v13, 0x42000000, v23
	v_mov_b32_e32 v11, 0
	v_cvt_pk_fp8_f32 v11, v12, v13
	v_mul_f32_e32 v15, 0x42000000, v21
	v_mul_f32_e32 v12, 0x42000000, v41
	v_mul_f32_e32 v13, 0x42000000, v43
	v_or_b32_e32 v44, s10, v31
	v_cvt_pk_fp8_f32 v10, v15, v18 op_sel:[0,0,1]
	v_cvt_pk_fp8_f32 v11, v12, v13 op_sel:[0,0,1]
	v_or_b32_e32 v12, s10, v32
	v_ashrrev_i32_e32 v45, 31, v44
	v_ashrrev_i32_e32 v13, 31, v12
	v_lshlrev_b64 v[44:45], 10, v[44:45]
	v_lshlrev_b64 v[12:13], 10, v[12:13]
	v_lshl_add_u64 v[44:45], v[16:17], 0, v[44:45]
	v_lshl_add_u64 v[12:13], v[16:17], 0, v[12:13]
	v_mov_b64_e32 v[224:225], v[44:45]
	v_mov_b64_e32 v[226:227], v[24:25]
	v_mov_b64_e32 v[228:229], v[12:13]
	v_mov_b64_e32 v[230:231], v[10:11]
	s_mov_b32 s100, 1
	s_waitcnt lgkmcnt(0)
	s_add_u32 s4, s4, s2
	s_addc_u32 s5, s5, s3
	v_cmp_gt_i64_e32 vcc, s[4:5], v[4:5]
	s_cbranch_vccz .LBB0_63
.LBB0_66:
	s_cmp_eq_u32 s100, 0
	s_cbranch_scc1 .Lp0d_j64_done
	global_store_dwordx2 v[216:217], v[218:219], off
	global_store_dwordx2 v[220:221], v[222:223], off
	global_store_dwordx2 v[224:225], v[226:227], off
	global_store_dwordx2 v[228:229], v[230:231], off
	s_mov_b32 s100, 0

; __global__ void __launch_bounds__(NWAVES * 64, 2) fwd_kernel(Args args) {
;     extern __shared__ __attribute__((aligned(16))) unsigned char lds[];
	.amdhsa_kernel _Z10fwd_kernel4Args
		.amdhsa_group_segment_fixed_size 16384
		.amdhsa_private_segment_fixed_size 0
		.amdhsa_kernarg_size 488
		.amdhsa_user_sgpr_count 2
		.amdhsa_user_sgpr_dispatch_ptr 0
		.amdhsa_user_sgpr_queue_ptr 0
		.amdhsa_user_sgpr_kernarg_segment_ptr 1
		.amdhsa_user_sgpr_dispatch_id 0
		.amdhsa_user_sgpr_kernarg_preload_length 0
		.amdhsa_user_sgpr_kernarg_preload_offset 0
		.amdhsa_user_sgpr_private_segment_size 0
		.amdhsa_uses_dynamic_stack 0
		.amdhsa_enable_private_segment 0
		.amdhsa_system_sgpr_workgroup_id_x 1
		.amdhsa_system_sgpr_workgroup_id_y 0
		.amdhsa_system_sgpr_workgroup_id_z 0
		.amdhsa_system_sgpr_workgroup_info 0
		.amdhsa_system_vgpr_workitem_id 0
		.amdhsa_next_free_vgpr 256
		.amdhsa_next_free_sgpr 102
		.amdhsa_accum_offset 256
		.amdhsa_reserve_vcc 1
		.amdhsa_float_round_mode_32 0
		.amdhsa_float_round_mode_16_64 0
		.amdhsa_float_denorm_mode_32 3
		.amdhsa_float_denorm_mode_16_64 3
		.amdhsa_dx10_clamp 1
		.amdhsa_ieee_mode 1
		.amdhsa_fp16_overflow 0
		.amdhsa_tg_split 0
		.amdhsa_exception_fp_ieee_invalid_op 0
		.amdhsa_exception_fp_denorm_src 0
		.amdhsa_exception_fp_ieee_div_zero 0
		.amdhsa_exception_fp_ieee_overflow 0
		.amdhsa_exception_fp_ieee_underflow 0
		.amdhsa_exception_fp_ieee_inexact 0
		.amdhsa_exception_int_div_zero 0
	.end_amdhsa_kernel

; __global__ void __launch_bounds__(NWAVES * 64, 2) fwd_kernel(Args args) {
;     extern __shared__ __attribute__((aligned(16))) unsigned char lds[];
amdhsa.kernels:
  - .agpr_count:     0
    .args:
      - .offset:         0
        .size:           232
        .value_kind:     by_value
      - .offset:         232
        .size:           4
        .value_kind:     hidden_block_count_x
      - .offset:         236
        .size:           4
        .value_kind:     hidden_block_count_y
      - .offset:         240
        .size:           4
        .value_kind:     hidden_block_count_z
      - .offset:         244
        .size:           2
        .value_kind:     hidden_group_size_x
      - .offset:         246
        .size:           2
        .value_kind:     hidden_group_size_y
      - .offset:         248
        .size:           2
        .value_kind:     hidden_group_size_z
      - .offset:         250
        .size:           2
        .value_kind:     hidden_remainder_x
      - .offset:         252
        .size:           2
        .value_kind:     hidden_remainder_y
      - .offset:         254
        .size:           2
        .value_kind:     hidden_remainder_z
      - .offset:         272
        .size:           8
        .value_kind:     hidden_global_offset_x
      - .offset:         280
        .size:           8
        .value_kind:     hidden_global_offset_y
      - .offset:         288
        .size:           8
        .value_kind:     hidden_global_offset_z
      - .offset:         296
        .size:           2
        .value_kind:     hidden_grid_dims
      - .offset:         352
        .size:           4
        .value_kind:     hidden_dynamic_lds_size
    .group_segment_fixed_size: 16384
    .kernarg_segment_align: 8
    .kernarg_segment_size: 488
    .language:       OpenCL C
    .language_version:
      - 2
      - 0
    .max_flat_workgroup_size: 512
    .name:           _Z10fwd_kernel4Args
    .private_segment_fixed_size: 0
    .sgpr_count:     108
    .sgpr_spill_count: 44
    .symbol:         _Z10fwd_kernel4Args.kd
    .uniform_work_group_size: 1
    .uses_dynamic_stack: false
    .vgpr_count:     256
    .vgpr_spill_count: 0
    .wavefront_size: 64
